# v12: v10 + weight-conversion tile loops de-serialised (wait for the next tile's loads moved to their first use)
# speedup vs baseline: 1.0044x; 1.0044x over previous
.LBB0_23:
	s_or_b64 exec, exec, s[4:5]
	v_lshlrev_b32_e32 v22, 4, v0
	s_add_u32 s14, s54, 0x1400000
	v_and_b32_e32 v22, 48, v22
	v_and_b32_e32 v23, 0x1fc, v0
	s_addc_u32 s15, s55, 0
	v_lshl_add_u32 v15, v1, 2, 0
	v_mul_u32_u24_e32 v17, 0x204, v16
	v_add_u32_e32 v23, 0, v23
	v_mul_u32_u24_e32 v24, 0x204, v22
	s_lshl_b32 s20, s33, 6
	v_mov_b32_e32 v14, 0
	v_lshrrev_b32_e32 v42, 2, v0
	s_lshl_b32 s19, s18, 6
	v_or_b32_e32 v43, s20, v16
	s_movk_i32 s21, 0x7ff
	s_movk_i32 s22, 0x800
	s_movk_i32 s23, 0x11f9
	s_movk_i32 s24, 0x4800
	s_movk_i32 s25, 0x11b9
	v_add_u32_e32 v44, v15, v17
	v_add_u32_e32 v45, v23, v24
	v_lshlrev_b32_e32 v38, 1, v22
	s_waitcnt vmcnt(0)
	s_branch .LBB0_26

.LBB0_25:
	ds_write2_b32 v44, v2, v3 offset1:1
	ds_write2_b32 v44, v4, v5 offset0:2 offset1:3
	ds_write2_b32 v44, v10, v11 offset0:4 offset1:5
	ds_write2_b32 v44, v12, v13 offset0:6 offset1:7
	ds_write2_b32 v44, v6, v7 offset0:64 offset1:65
	ds_write2_b32 v44, v8, v9 offset0:66 offset1:67
	ds_write2_b32 v44, v18, v19 offset0:68 offset1:69
	ds_write2_b32 v44, v20, v21 offset0:70 offset1:71
	v_add_u32_e32 v6, 0x800, v45
	s_waitcnt lgkmcnt(0)
	s_barrier
	v_add_u32_e32 v4, 0x400, v45
	ds_read2_b32 v[8:9], v6 offset0:4 offset1:133
	v_add_u32_e32 v6, 0xc00, v45
	ds_read2_b32 v[2:3], v45 offset1:129
	ds_read2_b32 v[4:5], v4 offset0:2 offset1:131
	ds_read2_b32 v[10:11], v6 offset0:6 offset1:135
	s_ashr_i32 s0, s18, 31
	s_lshr_b32 s0, s0, 27
	s_add_i32 s0, s18, s0
	s_ashr_i32 s0, s0, 5
	v_add_u32_e32 v15, 0x1800, v45
	v_add_u32_e32 v6, 0x1000, v45
	v_add_u32_e32 v12, 0x1400, v45
	ds_read2_b32 v[16:17], v15 offset0:12 offset1:141
	v_add_u32_e32 v15, 0x1c00, v45
	s_waitcnt lgkmcnt(3)
	v_cvt_pk_bf16_f32 v2, v2, v3
	s_waitcnt lgkmcnt(2)
	v_cvt_pk_bf16_f32 v3, v4, v5
	s_waitcnt lgkmcnt(1)
	v_cvt_pk_bf16_f32 v5, v10, v11
	v_lshl_or_b32 v10, s0, 7, v42
	ds_read2_b32 v[6:7], v6 offset0:8 offset1:137
	ds_read2_b32 v[12:13], v12 offset0:10 offset1:139
	ds_read2_b32 v[18:19], v15 offset0:14 offset1:143
	v_ashrrev_i32_e32 v11, 31, v10
	s_lshl_b32 s0, s0, 11
	v_lshlrev_b64 v[10:11], 12, v[10:11]
	s_sub_i32 s4, s19, s0
	v_lshl_add_u64 v[10:11], s[14:15], 0, v[10:11]
	s_ashr_i32 s5, s4, 31
	v_lshl_add_u64 v[10:11], s[4:5], 1, v[10:11]
	v_mov_b32_e32 v39, v14
	v_cvt_pk_bf16_f32 v4, v8, v9
	v_lshl_add_u64 v[10:11], v[10:11], 0, v[38:39]
	s_waitcnt lgkmcnt(2)
	v_cvt_pk_bf16_f32 v6, v6, v7
	s_waitcnt lgkmcnt(1)
	v_cvt_pk_bf16_f32 v7, v12, v13
	v_cvt_pk_bf16_f32 v8, v16, v17
	s_waitcnt lgkmcnt(0)
	v_cvt_pk_bf16_f32 v9, v18, v19
	global_store_dwordx4 v[10:11], v[2:5], off
	global_store_dwordx4 v[10:11], v[6:9], off offset:16
	s_waitcnt vmcnt(2)
	v_mov_b64_e32 v[10:11], v[26:27]
	v_mov_b64_e32 v[2:3], v[22:23]
	s_add_i32 s19, s19, s20
	s_andn2_b64 vcc, exec, s[16:17]
	v_mov_b64_e32 v[12:13], v[28:29]
	v_mov_b64_e32 v[4:5], v[24:25]
	s_mov_b32 s18, s26
	v_mov_b32_e32 v18, v34
	v_mov_b32_e32 v19, v35
	v_mov_b32_e32 v20, v36
	v_mov_b32_e32 v21, v37
	v_mov_b32_e32 v6, v30
	v_mov_b32_e32 v7, v31
	v_mov_b32_e32 v8, v32
	v_mov_b32_e32 v9, v33
	s_barrier
	s_cbranch_vccz .LBB0_31

.LBB0_37:
	s_or_b64 exec, exec, s[6:7]
	v_lshlrev_b32_e32 v10, 4, v0
	s_add_u32 s16, s54, 0x2600000
	v_and_b32_e32 v10, 48, v10
	v_and_b32_e32 v20, 0x1fc, v0
	s_addc_u32 s17, s55, 0
	v_lshl_add_u32 v18, v1, 2, 0
	v_mul_u32_u24_e32 v19, 0x204, v22
	v_add_u32_e32 v20, 0, v20
	v_mul_u32_u24_e32 v21, 0x204, v10
	s_lshl_b32 s22, s33, 6
	v_mov_b32_e32 v37, 0
	v_lshrrev_b32_e32 v34, 2, v0
	s_lshl_b32 s21, s20, 6
	v_or_b32_e32 v42, s22, v22
	s_movk_i32 s23, 0x7ff
	s_movk_i32 s24, 0x800
	s_movk_i32 s25, 0x7f9
	s_movk_i32 s26, 0x7b9
	v_add_u32_e32 v43, v18, v19
	v_add_u32_e32 v44, v20, v21
	v_lshlrev_b32_e32 v10, 1, v10
	s_waitcnt vmcnt(0)
	s_branch .LBB0_40

.LBB0_39:
	ds_write2_b32 v43, v2, v3 offset1:1
	ds_write2_b32 v43, v4, v5 offset0:2 offset1:3
	ds_write2_b32 v43, v6, v7 offset0:4 offset1:5
	ds_write2_b32 v43, v8, v9 offset0:6 offset1:7
	ds_write2_b32 v43, v35, v11 offset0:64 offset1:65
	ds_write2_b32 v43, v12, v13 offset0:66 offset1:67
	ds_write2_b32 v43, v14, v15 offset0:68 offset1:69
	ds_write2_b32 v43, v16, v17 offset0:70 offset1:71
	v_add_u32_e32 v6, 0x800, v44
	s_waitcnt lgkmcnt(0)
	s_barrier
	v_add_u32_e32 v4, 0x400, v44
	ds_read2_b32 v[8:9], v6 offset0:4 offset1:133
	v_add_u32_e32 v6, 0xc00, v44
	ds_read2_b32 v[2:3], v44 offset1:129
	ds_read2_b32 v[4:5], v4 offset0:2 offset1:131
	ds_read2_b32 v[12:13], v6 offset0:6 offset1:135
	s_ashr_i32 s0, s20, 31
	s_lshr_b32 s0, s0, 27
	v_add_u32_e32 v11, 0x1400, v44
	s_add_i32 s0, s20, s0
	ds_read2_b32 v[14:15], v11 offset0:10 offset1:139
	v_add_u32_e32 v11, 0x1800, v44
	s_ashr_i32 s0, s0, 5
	v_add_u32_e32 v6, 0x1000, v44
	ds_read2_b32 v[16:17], v11 offset0:12 offset1:141
	v_add_u32_e32 v11, 0x1c00, v44
	ds_read2_b32 v[6:7], v6 offset0:8 offset1:137
	ds_read2_b32 v[38:39], v11 offset0:14 offset1:143
	s_waitcnt lgkmcnt(6)
	v_cvt_pk_bf16_f32 v2, v2, v3
	s_waitcnt lgkmcnt(5)
	v_cvt_pk_bf16_f32 v3, v4, v5
	s_waitcnt lgkmcnt(4)
	v_cvt_pk_bf16_f32 v5, v12, v13
	v_lshl_or_b32 v12, s0, 7, v34
	v_ashrrev_i32_e32 v13, 31, v12
	s_lshl_b32 s0, s0, 11
	v_lshlrev_b64 v[12:13], 12, v[12:13]
	s_sub_i32 s6, s21, s0
	v_lshl_add_u64 v[12:13], s[16:17], 0, v[12:13]
	s_ashr_i32 s7, s6, 31
	v_lshl_add_u64 v[12:13], s[6:7], 1, v[12:13]
	v_mov_b32_e32 v11, v37
	s_waitcnt lgkmcnt(1)
	v_cvt_pk_bf16_f32 v6, v6, v7
	v_cvt_pk_bf16_f32 v7, v14, v15
	v_cvt_pk_bf16_f32 v4, v8, v9
	v_cvt_pk_bf16_f32 v8, v16, v17
	s_waitcnt lgkmcnt(0)
	v_cvt_pk_bf16_f32 v9, v38, v39
	v_lshl_add_u64 v[12:13], v[12:13], 0, v[10:11]
	global_store_dwordx4 v[12:13], v[2:5], off
	global_store_dwordx4 v[12:13], v[6:9], off offset:16
	s_add_i32 s21, s21, s22
	s_waitcnt vmcnt(2)
	v_mov_b64_e32 v[2:3], v[18:19]
	v_mov_b64_e32 v[6:7], v[22:23]
	s_andn2_b64 vcc, exec, s[18:19]
	v_mov_b64_e32 v[8:9], v[24:25]
	v_mov_b64_e32 v[4:5], v[20:21]
	s_mov_b32 s20, s27
	v_mov_b32_e32 v14, v30
	v_mov_b32_e32 v15, v31
	v_mov_b32_e32 v16, v32
	v_mov_b32_e32 v17, v33
	v_mov_b32_e32 v35, v26
	v_mov_b32_e32 v11, v27
	v_mov_b32_e32 v12, v28
	v_mov_b32_e32 v13, v29
	s_barrier
	s_cbranch_vccz .LBB0_45

.LBB0_51:
	s_or_b64 exec, exec, s[6:7]
	v_lshlrev_b32_e32 v10, 4, v0
	s_add_u32 s16, s54, 0x2e00000
	v_and_b32_e32 v10, 48, v10
	v_and_b32_e32 v20, 0x1fc, v0
	s_addc_u32 s17, s55, 0
	v_lshl_add_u32 v18, v1, 2, 0
	v_mul_u32_u24_e32 v19, 0x204, v22
	v_add_u32_e32 v20, 0, v20
	v_mul_u32_u24_e32 v21, 0x204, v10
	s_lshl_b32 s22, s33, 6
	v_mov_b32_e32 v37, 0
	v_lshrrev_b32_e32 v34, 2, v0
	s_lshl_b32 s21, s20, 6
	v_or_b32_e32 v42, s22, v22
	s_movk_i32 s23, 0x7ff
	s_movk_i32 s24, 0x800
	s_movk_i32 s25, 0x7f9
	s_movk_i32 s26, 0x7b9
	v_add_u32_e32 v43, v18, v19
	v_add_u32_e32 v44, v20, v21
	v_lshlrev_b32_e32 v10, 1, v10
	s_waitcnt vmcnt(0)
	s_branch .LBB0_54

.LBB0_65:
	s_or_b64 exec, exec, s[6:7]
	v_lshlrev_b32_e32 v10, 4, v0
	s_add_u32 s16, s54, 0x3600000
	v_and_b32_e32 v10, 48, v10
	v_and_b32_e32 v20, 0x1fc, v0
	s_addc_u32 s17, s55, 0
	v_lshl_add_u32 v18, v1, 2, 0
	v_mul_u32_u24_e32 v19, 0x204, v22
	v_add_u32_e32 v20, 0, v20
	v_mul_u32_u24_e32 v21, 0x204, v10
	s_lshl_b32 s22, s33, 6
	v_mov_b32_e32 v37, 0
	v_lshrrev_b32_e32 v34, 2, v0
	s_lshl_b32 s21, s20, 6
	v_or_b32_e32 v42, s22, v22
	s_movk_i32 s23, 0x7ff
	s_movk_i32 s24, 0x800
	s_movk_i32 s25, 0x7f9
	s_movk_i32 s26, 0x7b9
	v_add_u32_e32 v43, v18, v19
	v_add_u32_e32 v44, v20, v21
	v_lshlrev_b32_e32 v10, 1, v10
	s_waitcnt vmcnt(0)
	s_branch .LBB0_68

.LBB0_79:
	s_or_b64 exec, exec, s[6:7]
	v_lshlrev_b32_e32 v10, 4, v0
	s_add_u32 s16, s54, 0x3e00000
	v_and_b32_e32 v10, 48, v10
	v_and_b32_e32 v20, 0x1fc, v0
	s_addc_u32 s17, s55, 0
	v_lshl_add_u32 v18, v1, 2, 0
	v_mul_u32_u24_e32 v19, 0x204, v22
	v_add_u32_e32 v20, 0, v20
	v_mul_u32_u24_e32 v21, 0x204, v10
	s_lshl_b32 s22, s33, 6
	v_mov_b32_e32 v37, 0
	v_lshrrev_b32_e32 v34, 2, v0
	s_lshl_b32 s21, s20, 6
	v_or_b32_e32 v42, s22, v22
	s_movk_i32 s23, 0x7ff
	s_movk_i32 s24, 0x800
	s_movk_i32 s25, 0x7f9
	s_movk_i32 s26, 0x7b9
	v_add_u32_e32 v43, v18, v19
	v_add_u32_e32 v44, v20, v21
	v_lshlrev_b32_e32 v10, 1, v10
	s_waitcnt vmcnt(0)
	s_branch .LBB0_82

.LBB0_93:
	s_or_b64 exec, exec, s[6:7]
	v_lshlrev_b32_e32 v10, 4, v0
	s_add_u32 s16, s54, 0x4600000
	v_and_b32_e32 v10, 48, v10
	v_and_b32_e32 v20, 0x1fc, v0
	s_addc_u32 s17, s55, 0
	v_lshl_add_u32 v18, v1, 2, 0
	v_mul_u32_u24_e32 v19, 0x204, v22
	v_add_u32_e32 v20, 0, v20
	v_mul_u32_u24_e32 v21, 0x204, v10
	s_lshl_b32 s22, s33, 6
	v_mov_b32_e32 v37, 0
	v_lshrrev_b32_e32 v34, 2, v0
	s_lshl_b32 s21, s20, 6
	v_or_b32_e32 v42, s22, v22
	s_movk_i32 s23, 0x7ff
	s_movk_i32 s24, 0x800
	s_movk_i32 s25, 0x7f9
	s_movk_i32 s26, 0x7b9
	v_add_u32_e32 v43, v18, v19
	v_add_u32_e32 v44, v20, v21
	v_lshlrev_b32_e32 v10, 1, v10
	s_waitcnt vmcnt(0)
	s_branch .LBB0_96

.LBB0_107:
	s_or_b64 exec, exec, s[8:9]
	v_lshlrev_b32_e32 v16, 2, v1
	v_mov_b32_e32 v14, 0
	s_add_u32 s8, s54, 0x4e00000
	v_add_u32_e32 v15, 0, v16
	v_lshl_add_u32 v22, v42, 2, 0
	v_mov_b32_e32 v17, v14
	s_addc_u32 s9, s55, 0
	s_waitcnt lgkmcnt(0)
	v_lshl_add_u64 v[38:39], s[14:15], 0, v[16:17]
	s_lshl_b32 s21, s20, 6
	s_lshl_b32 s22, s33, 6
	s_movk_i32 s23, 0x800
	s_movk_i32 s24, 0x180
	v_add_u32_e32 v47, v15, v43
	v_add_u32_e32 v48, v22, v46
	v_lshlrev_b32_e32 v40, 1, v45
	s_waitcnt vmcnt(0)
	s_branch .LBB0_110

.LBB0_109:
	ds_write2_b32 v47, v2, v3 offset1:1
	ds_write2_b32 v47, v4, v5 offset0:2 offset1:3
	ds_write2_b32 v47, v10, v11 offset0:4 offset1:5
	ds_write2_b32 v47, v12, v13 offset0:6 offset1:7
	ds_write2_b32 v47, v6, v7 offset0:64 offset1:65
	ds_write2_b32 v47, v8, v9 offset0:66 offset1:67
	ds_write2_b32 v47, v18, v19 offset0:68 offset1:69
	ds_write2_b32 v47, v20, v21 offset0:70 offset1:71
	v_add_u32_e32 v6, 0x800, v48
	s_waitcnt lgkmcnt(0)
	s_barrier
	v_add_u32_e32 v4, 0x400, v48
	ds_read2_b32 v[8:9], v6 offset0:4 offset1:133
	v_add_u32_e32 v6, 0xc00, v48
	ds_read2_b32 v[2:3], v48 offset1:129
	ds_read2_b32 v[4:5], v4 offset0:2 offset1:131
	ds_read2_b32 v[10:11], v6 offset0:6 offset1:135
	s_ashr_i32 s0, s20, 31
	s_lshr_b32 s0, s0, 27
	s_add_i32 s0, s20, s0
	s_ashr_i32 s0, s0, 5
	v_add_u32_e32 v15, 0x1800, v48
	v_add_u32_e32 v6, 0x1000, v48
	v_add_u32_e32 v12, 0x1400, v48
	ds_read2_b32 v[16:17], v15 offset0:12 offset1:141
	v_add_u32_e32 v15, 0x1c00, v48
	s_waitcnt lgkmcnt(3)
	v_cvt_pk_bf16_f32 v2, v2, v3
	s_waitcnt lgkmcnt(2)
	v_cvt_pk_bf16_f32 v3, v4, v5
	s_waitcnt lgkmcnt(1)
	v_cvt_pk_bf16_f32 v5, v10, v11
	v_lshl_or_b32 v10, s0, 7, v42
	ds_read2_b32 v[6:7], v6 offset0:8 offset1:137
	ds_read2_b32 v[12:13], v12 offset0:10 offset1:139
	ds_read2_b32 v[18:19], v15 offset0:14 offset1:143
	v_ashrrev_i32_e32 v11, 31, v10
	s_lshl_b32 s0, s0, 11
	v_lshlrev_b64 v[10:11], 12, v[10:11]
	s_sub_i32 s16, s21, s0
	v_lshl_add_u64 v[10:11], s[8:9], 0, v[10:11]
	s_ashr_i32 s17, s16, 31
	v_lshl_add_u64 v[10:11], s[16:17], 1, v[10:11]
	v_mov_b32_e32 v41, v14
	v_cvt_pk_bf16_f32 v4, v8, v9
	v_lshl_add_u64 v[10:11], v[10:11], 0, v[40:41]
	s_waitcnt lgkmcnt(2)
	v_cvt_pk_bf16_f32 v6, v6, v7
	s_waitcnt lgkmcnt(1)
	v_cvt_pk_bf16_f32 v7, v12, v13
	v_cvt_pk_bf16_f32 v8, v16, v17
	s_waitcnt lgkmcnt(0)
	v_cvt_pk_bf16_f32 v9, v18, v19
	global_store_dwordx4 v[10:11], v[2:5], off
	global_store_dwordx4 v[10:11], v[6:9], off offset:16
	s_waitcnt vmcnt(2)
	v_mov_b64_e32 v[10:11], v[26:27]
	v_mov_b64_e32 v[2:3], v[22:23]
	s_add_i32 s21, s21, s22
	s_andn2_b64 vcc, exec, s[10:11]
	v_mov_b64_e32 v[12:13], v[28:29]
	v_mov_b64_e32 v[4:5], v[24:25]
	s_mov_b32 s20, s25
	v_mov_b32_e32 v18, v34
	v_mov_b32_e32 v19, v35
	v_mov_b32_e32 v20, v36
	v_mov_b32_e32 v21, v37
	v_mov_b32_e32 v6, v30
	v_mov_b32_e32 v7, v31
	v_mov_b32_e32 v8, v32
	v_mov_b32_e32 v9, v33
	s_barrier
	s_cbranch_vccz .LBB0_115

.LBB0_121:
	s_or_b64 exec, exec, s[8:9]
	v_lshlrev_b32_e32 v16, 2, v1
	v_mov_b32_e32 v14, 0
	s_add_u32 s8, s54, 0x4f00000
	v_add_u32_e32 v15, 0, v16
	v_lshl_add_u32 v22, v42, 2, 0
	v_mov_b32_e32 v17, v14
	s_addc_u32 s9, s55, 0
	s_waitcnt lgkmcnt(0)
	v_lshl_add_u64 v[38:39], s[16:17], 0, v[16:17]
	s_lshl_b32 s23, s22, 6
	s_lshl_b32 s24, s33, 6
	s_movk_i32 s25, 0x800
	s_movk_i32 s26, 0x180
	v_add_u32_e32 v47, v15, v43
	v_add_u32_e32 v48, v22, v46
	v_lshlrev_b32_e32 v40, 1, v45
	s_waitcnt vmcnt(0)
	s_branch .LBB0_124

.LBB0_123:
	ds_write2_b32 v47, v2, v3 offset1:1
	ds_write2_b32 v47, v4, v5 offset0:2 offset1:3
	ds_write2_b32 v47, v10, v11 offset0:4 offset1:5
	ds_write2_b32 v47, v12, v13 offset0:6 offset1:7
	ds_write2_b32 v47, v6, v7 offset0:64 offset1:65
	ds_write2_b32 v47, v8, v9 offset0:66 offset1:67
	ds_write2_b32 v47, v18, v19 offset0:68 offset1:69
	ds_write2_b32 v47, v20, v21 offset0:70 offset1:71
	v_add_u32_e32 v6, 0x800, v48
	s_waitcnt lgkmcnt(0)
	s_barrier
	v_add_u32_e32 v4, 0x400, v48
	ds_read2_b32 v[8:9], v6 offset0:4 offset1:133
	v_add_u32_e32 v6, 0xc00, v48
	ds_read2_b32 v[2:3], v48 offset1:129
	ds_read2_b32 v[4:5], v4 offset0:2 offset1:131
	ds_read2_b32 v[10:11], v6 offset0:6 offset1:135
	s_ashr_i32 s0, s22, 31
	s_lshr_b32 s0, s0, 27
	s_add_i32 s0, s22, s0
	s_ashr_i32 s0, s0, 5
	v_add_u32_e32 v15, 0x1800, v48
	v_add_u32_e32 v6, 0x1000, v48
	v_add_u32_e32 v12, 0x1400, v48
	ds_read2_b32 v[16:17], v15 offset0:12 offset1:141
	v_add_u32_e32 v15, 0x1c00, v48
	s_waitcnt lgkmcnt(3)
	v_cvt_pk_bf16_f32 v2, v2, v3
	s_waitcnt lgkmcnt(2)
	v_cvt_pk_bf16_f32 v3, v4, v5
	s_waitcnt lgkmcnt(1)
	v_cvt_pk_bf16_f32 v5, v10, v11
	v_lshl_or_b32 v10, s0, 7, v42
	ds_read2_b32 v[6:7], v6 offset0:8 offset1:137
	ds_read2_b32 v[12:13], v12 offset0:10 offset1:139
	ds_read2_b32 v[18:19], v15 offset0:14 offset1:143
	v_ashrrev_i32_e32 v11, 31, v10
	s_lshl_b32 s0, s0, 11
	v_lshlrev_b64 v[10:11], 12, v[10:11]
	s_sub_i32 s18, s23, s0
	v_lshl_add_u64 v[10:11], s[8:9], 0, v[10:11]
	s_ashr_i32 s19, s18, 31
	v_lshl_add_u64 v[10:11], s[18:19], 1, v[10:11]
	v_mov_b32_e32 v41, v14
	v_cvt_pk_bf16_f32 v4, v8, v9
	v_lshl_add_u64 v[10:11], v[10:11], 0, v[40:41]
	s_waitcnt lgkmcnt(2)
	v_cvt_pk_bf16_f32 v6, v6, v7
	s_waitcnt lgkmcnt(1)
	v_cvt_pk_bf16_f32 v7, v12, v13
	v_cvt_pk_bf16_f32 v8, v16, v17
	s_waitcnt lgkmcnt(0)
	v_cvt_pk_bf16_f32 v9, v18, v19
	global_store_dwordx4 v[10:11], v[2:5], off
	global_store_dwordx4 v[10:11], v[6:9], off offset:16
	s_waitcnt vmcnt(2)
	v_mov_b64_e32 v[10:11], v[26:27]
	v_mov_b64_e32 v[2:3], v[22:23]
	s_add_i32 s23, s23, s24
	s_andn2_b64 vcc, exec, s[10:11]
	v_mov_b64_e32 v[12:13], v[28:29]
	v_mov_b64_e32 v[4:5], v[24:25]
	s_mov_b32 s22, s27
	v_mov_b32_e32 v18, v34
	v_mov_b32_e32 v19, v35
	v_mov_b32_e32 v20, v36
	v_mov_b32_e32 v21, v37
	v_mov_b32_e32 v6, v30
	v_mov_b32_e32 v7, v31
	v_mov_b32_e32 v8, v32
	v_mov_b32_e32 v9, v33
	s_barrier
	s_cbranch_vccz .LBB0_129

.LBB0_135:
	s_or_b64 exec, exec, s[8:9]
	s_add_u32 s20, s54, 0x5100000
	s_addc_u32 s21, s55, 0
	v_lshl_add_u32 v10, v1, 2, 0
	v_lshl_add_u32 v18, v42, 2, 0
	s_lshl_b32 s26, s33, 6
	v_mov_b32_e32 v37, 0
	s_lshl_b32 s25, s24, 6
	v_or_b32_e32 v34, s26, v44
	s_movk_i32 s27, 0x5f
	s_movk_i32 s28, 0x60
	s_movk_i32 s29, 0x800
	s_movk_i32 s30, 0x7b9
	v_add_u32_e32 v47, v10, v43
	v_add_u32_e32 v48, v18, v46
	v_lshlrev_b32_e32 v10, 1, v45
	s_waitcnt vmcnt(0)
	s_branch .LBB0_138

.LBB0_137:
	ds_write2_b32 v47, v2, v3 offset1:1
	ds_write2_b32 v47, v4, v5 offset0:2 offset1:3
	ds_write2_b32 v47, v6, v7 offset0:4 offset1:5
	ds_write2_b32 v47, v8, v9 offset0:6 offset1:7
	ds_write2_b32 v47, v35, v11 offset0:64 offset1:65
	ds_write2_b32 v47, v12, v13 offset0:66 offset1:67
	ds_write2_b32 v47, v14, v15 offset0:68 offset1:69
	ds_write2_b32 v47, v16, v17 offset0:70 offset1:71
	v_add_u32_e32 v6, 0x800, v48
	s_waitcnt lgkmcnt(0)
	s_barrier
	v_add_u32_e32 v4, 0x400, v48
	ds_read2_b32 v[8:9], v6 offset0:4 offset1:133
	v_add_u32_e32 v6, 0xc00, v48
	ds_read2_b32 v[2:3], v48 offset1:129
	ds_read2_b32 v[4:5], v4 offset0:2 offset1:131
	ds_read2_b32 v[12:13], v6 offset0:6 offset1:135
	s_lshr_b32 s0, s24, 31
	s_add_i32 s0, s24, s0
	v_add_u32_e32 v11, 0x1400, v48
	ds_read2_b32 v[14:15], v11 offset0:10 offset1:139
	v_add_u32_e32 v11, 0x1800, v48
	s_lshl_b32 s0, s0, 6
	v_add_u32_e32 v6, 0x1000, v48
	ds_read2_b32 v[16:17], v11 offset0:12 offset1:141
	v_add_u32_e32 v11, 0x1c00, v48
	s_and_b32 s0, s0, 0xffffff80
	ds_read2_b32 v[6:7], v6 offset0:8 offset1:137
	ds_read2_b32 v[38:39], v11 offset0:14 offset1:143
	s_waitcnt lgkmcnt(6)
	v_cvt_pk_bf16_f32 v2, v2, v3
	s_waitcnt lgkmcnt(5)
	v_cvt_pk_bf16_f32 v3, v4, v5
	s_waitcnt lgkmcnt(4)
	v_cvt_pk_bf16_f32 v5, v12, v13
	v_or_b32_e32 v12, s0, v42
	v_ashrrev_i32_e32 v13, 31, v12
	v_lshlrev_b64 v[12:13], 8, v[12:13]
	s_sub_i32 s8, s25, s0
	v_lshl_add_u64 v[12:13], s[20:21], 0, v[12:13]
	s_ashr_i32 s9, s8, 31
	v_lshl_add_u64 v[12:13], s[8:9], 1, v[12:13]
	v_mov_b32_e32 v11, v37
	s_waitcnt lgkmcnt(1)
	v_cvt_pk_bf16_f32 v6, v6, v7
	v_cvt_pk_bf16_f32 v7, v14, v15
	v_cvt_pk_bf16_f32 v4, v8, v9
	v_cvt_pk_bf16_f32 v8, v16, v17
	s_waitcnt lgkmcnt(0)
	v_cvt_pk_bf16_f32 v9, v38, v39
	v_lshl_add_u64 v[12:13], v[12:13], 0, v[10:11]
	global_store_dwordx4 v[12:13], v[2:5], off
	global_store_dwordx4 v[12:13], v[6:9], off offset:16
	s_add_i32 s25, s25, s26
	s_waitcnt vmcnt(2)
	v_mov_b64_e32 v[2:3], v[18:19]
	v_mov_b64_e32 v[6:7], v[22:23]
	s_andn2_b64 vcc, exec, s[22:23]
	v_mov_b64_e32 v[8:9], v[24:25]
	v_mov_b64_e32 v[4:5], v[20:21]
	s_mov_b32 s24, s31
	v_mov_b32_e32 v14, v30
	v_mov_b32_e32 v15, v31
	v_mov_b32_e32 v16, v32
	v_mov_b32_e32 v17, v33
	v_mov_b32_e32 v35, v26
	v_mov_b32_e32 v11, v27
	v_mov_b32_e32 v12, v28
	v_mov_b32_e32 v13, v29
	s_barrier
	s_cbranch_vccz .LBB0_143

.LBB0_149:
	s_or_b64 exec, exec, s[4:5]
	s_add_u32 s20, s54, 0x5300000
	s_addc_u32 s21, s55, 0
	v_lshl_add_u32 v10, v1, 2, 0
	v_lshl_add_u32 v18, v42, 2, 0
	s_lshl_b32 s30, s33, 6
	v_mov_b32_e32 v37, 0
	s_lshl_b32 s29, s28, 6
	v_or_b32_e32 v34, s30, v44
	s_movk_i32 s31, 0x5f
	s_movk_i32 s34, 0x60
	s_movk_i32 s35, 0x800
	s_movk_i32 s36, 0x7b9
	v_add_u32_e32 v47, v10, v43
	v_add_u32_e32 v48, v18, v46
	v_lshlrev_b32_e32 v10, 1, v45
	s_waitcnt vmcnt(0)
	s_branch .LBB0_152

.LBB0_151:
	ds_write2_b32 v47, v2, v3 offset1:1
	ds_write2_b32 v47, v4, v5 offset0:2 offset1:3
	ds_write2_b32 v47, v6, v7 offset0:4 offset1:5
	ds_write2_b32 v47, v8, v9 offset0:6 offset1:7
	ds_write2_b32 v47, v35, v11 offset0:64 offset1:65
	ds_write2_b32 v47, v12, v13 offset0:66 offset1:67
	ds_write2_b32 v47, v14, v15 offset0:68 offset1:69
	ds_write2_b32 v47, v16, v17 offset0:70 offset1:71
	v_add_u32_e32 v6, 0x800, v48
	s_waitcnt lgkmcnt(0)
	s_barrier
	v_add_u32_e32 v4, 0x400, v48
	ds_read2_b32 v[8:9], v6 offset0:4 offset1:133
	v_add_u32_e32 v6, 0xc00, v48
	ds_read2_b32 v[2:3], v48 offset1:129
	ds_read2_b32 v[4:5], v4 offset0:2 offset1:131
	ds_read2_b32 v[12:13], v6 offset0:6 offset1:135
	s_lshr_b32 s0, s28, 31
	s_add_i32 s0, s28, s0
	v_add_u32_e32 v11, 0x1400, v48
	ds_read2_b32 v[14:15], v11 offset0:10 offset1:139
	v_add_u32_e32 v11, 0x1800, v48
	s_lshl_b32 s0, s0, 6
	v_add_u32_e32 v6, 0x1000, v48
	ds_read2_b32 v[16:17], v11 offset0:12 offset1:141
	v_add_u32_e32 v11, 0x1c00, v48
	s_and_b32 s0, s0, 0xffffff80
	ds_read2_b32 v[6:7], v6 offset0:8 offset1:137
	ds_read2_b32 v[38:39], v11 offset0:14 offset1:143
	s_waitcnt lgkmcnt(6)
	v_cvt_pk_bf16_f32 v2, v2, v3
	s_waitcnt lgkmcnt(5)
	v_cvt_pk_bf16_f32 v3, v4, v5
	s_waitcnt lgkmcnt(4)
	v_cvt_pk_bf16_f32 v5, v12, v13
	v_or_b32_e32 v12, s0, v42
	v_ashrrev_i32_e32 v13, 31, v12
	v_lshlrev_b64 v[12:13], 8, v[12:13]
	s_sub_i32 s4, s29, s0
	v_lshl_add_u64 v[12:13], s[20:21], 0, v[12:13]
	s_ashr_i32 s5, s4, 31
	v_lshl_add_u64 v[12:13], s[4:5], 1, v[12:13]
	v_mov_b32_e32 v11, v37
	s_waitcnt lgkmcnt(1)
	v_cvt_pk_bf16_f32 v6, v6, v7
	v_cvt_pk_bf16_f32 v7, v14, v15
	v_cvt_pk_bf16_f32 v4, v8, v9
	v_cvt_pk_bf16_f32 v8, v16, v17
	s_waitcnt lgkmcnt(0)
	v_cvt_pk_bf16_f32 v9, v38, v39
	v_lshl_add_u64 v[12:13], v[12:13], 0, v[10:11]
	global_store_dwordx4 v[12:13], v[2:5], off
	global_store_dwordx4 v[12:13], v[6:9], off offset:16
	s_add_i32 s29, s29, s30
	s_waitcnt vmcnt(2)
	v_mov_b64_e32 v[2:3], v[18:19]
	v_mov_b64_e32 v[6:7], v[22:23]
	s_andn2_b64 vcc, exec, s[22:23]
	v_mov_b64_e32 v[8:9], v[24:25]
	v_mov_b64_e32 v[4:5], v[20:21]
	s_mov_b32 s28, s37
	v_mov_b32_e32 v14, v30
	v_mov_b32_e32 v15, v31
	v_mov_b32_e32 v16, v32
	v_mov_b32_e32 v17, v33
	v_mov_b32_e32 v35, v26
	v_mov_b32_e32 v11, v27
	v_mov_b32_e32 v12, v28
	v_mov_b32_e32 v13, v29
	s_barrier
	s_cbranch_vccz .LBB0_157

.LBB0_162:
	s_or_b64 exec, exec, s[4:5]
	v_lshlrev_b32_e32 v16, 2, v1
	v_mov_b32_e32 v14, 0
	s_add_u32 s4, s54, 0x4e80000
	v_add_u32_e32 v15, 0, v16
	v_lshl_add_u32 v22, v42, 2, 0
	v_mov_b32_e32 v17, v14
	s_addc_u32 s5, s55, 0
	v_lshl_add_u64 v[38:39], s[8:9], 0, v[16:17]
	s_lshl_b32 s27, s26, 6
	s_lshl_b32 s28, s33, 6
	s_movk_i32 s29, 0x800
	s_movk_i32 s30, 0x180
	v_add_u32_e32 v47, v15, v43
	v_add_u32_e32 v48, v22, v46
	v_lshlrev_b32_e32 v40, 1, v45
	s_waitcnt vmcnt(0)
	s_branch .LBB0_165

.LBB0_164:
	ds_write2_b32 v47, v2, v3 offset1:1
	ds_write2_b32 v47, v4, v5 offset0:2 offset1:3
	ds_write2_b32 v47, v10, v11 offset0:4 offset1:5
	ds_write2_b32 v47, v12, v13 offset0:6 offset1:7
	ds_write2_b32 v47, v6, v7 offset0:64 offset1:65
	ds_write2_b32 v47, v8, v9 offset0:66 offset1:67
	ds_write2_b32 v47, v18, v19 offset0:68 offset1:69
	ds_write2_b32 v47, v20, v21 offset0:70 offset1:71
	v_add_u32_e32 v6, 0x800, v48
	s_waitcnt lgkmcnt(0)
	s_barrier
	v_add_u32_e32 v4, 0x400, v48
	ds_read2_b32 v[8:9], v6 offset0:4 offset1:133
	v_add_u32_e32 v6, 0xc00, v48
	ds_read2_b32 v[2:3], v48 offset1:129
	ds_read2_b32 v[4:5], v4 offset0:2 offset1:131
	ds_read2_b32 v[10:11], v6 offset0:6 offset1:135
	s_ashr_i32 s0, s26, 31
	s_lshr_b32 s0, s0, 27
	s_add_i32 s0, s26, s0
	s_ashr_i32 s0, s0, 5
	v_add_u32_e32 v15, 0x1800, v48
	v_add_u32_e32 v6, 0x1000, v48
	v_add_u32_e32 v12, 0x1400, v48
	ds_read2_b32 v[16:17], v15 offset0:12 offset1:141
	v_add_u32_e32 v15, 0x1c00, v48
	s_waitcnt lgkmcnt(3)
	v_cvt_pk_bf16_f32 v2, v2, v3
	s_waitcnt lgkmcnt(2)
	v_cvt_pk_bf16_f32 v3, v4, v5
	s_waitcnt lgkmcnt(1)
	v_cvt_pk_bf16_f32 v5, v10, v11
	v_lshl_or_b32 v10, s0, 7, v42
	ds_read2_b32 v[6:7], v6 offset0:8 offset1:137
	ds_read2_b32 v[12:13], v12 offset0:10 offset1:139
	ds_read2_b32 v[18:19], v15 offset0:14 offset1:143
	v_ashrrev_i32_e32 v11, 31, v10
	s_lshl_b32 s0, s0, 11
	v_lshlrev_b64 v[10:11], 12, v[10:11]
	s_sub_i32 s14, s27, s0
	v_lshl_add_u64 v[10:11], s[4:5], 0, v[10:11]
	s_ashr_i32 s15, s14, 31
	v_lshl_add_u64 v[10:11], s[14:15], 1, v[10:11]
	v_mov_b32_e32 v41, v14
	v_cvt_pk_bf16_f32 v4, v8, v9
	v_lshl_add_u64 v[10:11], v[10:11], 0, v[40:41]
	s_waitcnt lgkmcnt(2)
	v_cvt_pk_bf16_f32 v6, v6, v7
	s_waitcnt lgkmcnt(1)
	v_cvt_pk_bf16_f32 v7, v12, v13
	v_cvt_pk_bf16_f32 v8, v16, v17
	s_waitcnt lgkmcnt(0)
	v_cvt_pk_bf16_f32 v9, v18, v19
	global_store_dwordx4 v[10:11], v[2:5], off
	global_store_dwordx4 v[10:11], v[6:9], off offset:16
	s_waitcnt vmcnt(2)
	v_mov_b64_e32 v[10:11], v[26:27]
	v_mov_b64_e32 v[2:3], v[22:23]
	s_add_i32 s27, s27, s28
	s_andn2_b64 vcc, exec, s[8:9]
	v_mov_b64_e32 v[12:13], v[28:29]
	v_mov_b64_e32 v[4:5], v[24:25]
	s_mov_b32 s26, s31
	v_mov_b32_e32 v18, v34
	v_mov_b32_e32 v19, v35
	v_mov_b32_e32 v20, v36
	v_mov_b32_e32 v21, v37
	v_mov_b32_e32 v6, v30
	v_mov_b32_e32 v7, v31
	v_mov_b32_e32 v8, v32
	v_mov_b32_e32 v9, v33
	s_barrier
	s_cbranch_vccz .LBB0_170

.LBB0_175:
	s_or_b64 exec, exec, s[4:5]
	v_mov_b32_e32 v14, 0
	s_add_u32 s4, s54, 0x4f80000
	v_add_u32_e32 v15, 0, v16
	v_lshl_add_u32 v22, v42, 2, 0
	v_mov_b32_e32 v17, v14
	s_addc_u32 s5, s55, 0
	v_lshl_add_u64 v[38:39], s[8:9], 0, v[16:17]
	s_lshl_b32 s23, s22, 6
	s_lshl_b32 s26, s33, 6
	s_movk_i32 s27, 0x800
	s_movk_i32 s28, 0x180
	v_add_u32_e32 v47, v15, v43
	v_add_u32_e32 v48, v22, v46
	v_lshlrev_b32_e32 v40, 1, v45
	s_waitcnt vmcnt(0)
	s_branch .LBB0_178

.LBB0_177:
	ds_write2_b32 v47, v2, v3 offset1:1
	ds_write2_b32 v47, v4, v5 offset0:2 offset1:3
	ds_write2_b32 v47, v10, v11 offset0:4 offset1:5
	ds_write2_b32 v47, v12, v13 offset0:6 offset1:7
	ds_write2_b32 v47, v6, v7 offset0:64 offset1:65
	ds_write2_b32 v47, v8, v9 offset0:66 offset1:67
	ds_write2_b32 v47, v18, v19 offset0:68 offset1:69
	ds_write2_b32 v47, v20, v21 offset0:70 offset1:71
	v_add_u32_e32 v6, 0x800, v48
	s_waitcnt lgkmcnt(0)
	s_barrier
	v_add_u32_e32 v4, 0x400, v48
	ds_read2_b32 v[8:9], v6 offset0:4 offset1:133
	v_add_u32_e32 v6, 0xc00, v48
	ds_read2_b32 v[2:3], v48 offset1:129
	ds_read2_b32 v[4:5], v4 offset0:2 offset1:131
	ds_read2_b32 v[10:11], v6 offset0:6 offset1:135
	s_ashr_i32 s0, s22, 31
	s_lshr_b32 s0, s0, 27
	s_add_i32 s0, s22, s0
	s_ashr_i32 s0, s0, 5
	v_add_u32_e32 v15, 0x1800, v48
	v_add_u32_e32 v6, 0x1000, v48
	v_add_u32_e32 v12, 0x1400, v48
	ds_read2_b32 v[16:17], v15 offset0:12 offset1:141
	v_add_u32_e32 v15, 0x1c00, v48
	s_waitcnt lgkmcnt(3)
	v_cvt_pk_bf16_f32 v2, v2, v3
	s_waitcnt lgkmcnt(2)
	v_cvt_pk_bf16_f32 v3, v4, v5
	s_waitcnt lgkmcnt(1)
	v_cvt_pk_bf16_f32 v5, v10, v11
	v_lshl_or_b32 v10, s0, 7, v42
	ds_read2_b32 v[6:7], v6 offset0:8 offset1:137
	ds_read2_b32 v[12:13], v12 offset0:10 offset1:139
	ds_read2_b32 v[18:19], v15 offset0:14 offset1:143
	v_ashrrev_i32_e32 v11, 31, v10
	s_lshl_b32 s0, s0, 11
	v_lshlrev_b64 v[10:11], 12, v[10:11]
	s_sub_i32 s14, s23, s0
	v_lshl_add_u64 v[10:11], s[4:5], 0, v[10:11]
	s_ashr_i32 s15, s14, 31
	v_lshl_add_u64 v[10:11], s[14:15], 1, v[10:11]
	v_mov_b32_e32 v41, v14
	v_cvt_pk_bf16_f32 v4, v8, v9
	v_lshl_add_u64 v[10:11], v[10:11], 0, v[40:41]
	s_waitcnt lgkmcnt(2)
	v_cvt_pk_bf16_f32 v6, v6, v7
	s_waitcnt lgkmcnt(1)
	v_cvt_pk_bf16_f32 v7, v12, v13
	v_cvt_pk_bf16_f32 v8, v16, v17
	s_waitcnt lgkmcnt(0)
	v_cvt_pk_bf16_f32 v9, v18, v19
	global_store_dwordx4 v[10:11], v[2:5], off
	global_store_dwordx4 v[10:11], v[6:9], off offset:16
	s_waitcnt vmcnt(2)
	v_mov_b64_e32 v[10:11], v[26:27]
	v_mov_b64_e32 v[2:3], v[22:23]
	s_add_i32 s23, s23, s26
	s_andn2_b64 vcc, exec, s[8:9]
	v_mov_b64_e32 v[12:13], v[28:29]
	v_mov_b64_e32 v[4:5], v[24:25]
	s_mov_b32 s22, s29
	v_mov_b32_e32 v18, v34
	v_mov_b32_e32 v19, v35
	v_mov_b32_e32 v20, v36
	v_mov_b32_e32 v21, v37
	v_mov_b32_e32 v6, v30
	v_mov_b32_e32 v7, v31
	v_mov_b32_e32 v8, v32
	v_mov_b32_e32 v9, v33
	s_barrier
	s_cbranch_vccz .LBB0_183

.LBB0_188:
	s_or_b64 exec, exec, s[4:5]
	s_add_u32 s14, s54, 0x5180000
	s_addc_u32 s15, s55, 0
	v_lshl_add_u32 v10, v1, 2, 0
	v_lshl_add_u32 v18, v42, 2, 0
	s_lshl_b32 s19, s33, 6
	v_mov_b32_e32 v37, 0
	s_lshl_b32 s18, s22, 6
	v_or_b32_e32 v34, s19, v44
	s_movk_i32 s23, 0x5f
	s_movk_i32 s26, 0x60
	s_movk_i32 s27, 0x800
	s_movk_i32 s28, 0x7b9
	v_add_u32_e32 v47, v10, v43
	v_add_u32_e32 v48, v18, v46
	v_lshlrev_b32_e32 v10, 1, v45
	s_waitcnt vmcnt(0)
	s_branch .LBB0_191

.LBB0_190:
	ds_write2_b32 v47, v2, v3 offset1:1
	ds_write2_b32 v47, v4, v5 offset0:2 offset1:3
	ds_write2_b32 v47, v6, v7 offset0:4 offset1:5
	ds_write2_b32 v47, v8, v9 offset0:6 offset1:7
	ds_write2_b32 v47, v35, v11 offset0:64 offset1:65
	ds_write2_b32 v47, v12, v13 offset0:66 offset1:67
	ds_write2_b32 v47, v14, v15 offset0:68 offset1:69
	ds_write2_b32 v47, v16, v17 offset0:70 offset1:71
	v_add_u32_e32 v6, 0x800, v48
	s_waitcnt lgkmcnt(0)
	s_barrier
	v_add_u32_e32 v4, 0x400, v48
	ds_read2_b32 v[8:9], v6 offset0:4 offset1:133
	v_add_u32_e32 v6, 0xc00, v48
	ds_read2_b32 v[2:3], v48 offset1:129
	ds_read2_b32 v[4:5], v4 offset0:2 offset1:131
	ds_read2_b32 v[12:13], v6 offset0:6 offset1:135
	s_lshr_b32 s0, s22, 31
	s_add_i32 s0, s22, s0
	v_add_u32_e32 v11, 0x1400, v48
	ds_read2_b32 v[14:15], v11 offset0:10 offset1:139
	v_add_u32_e32 v11, 0x1800, v48
	s_lshl_b32 s0, s0, 6
	v_add_u32_e32 v6, 0x1000, v48
	ds_read2_b32 v[16:17], v11 offset0:12 offset1:141
	v_add_u32_e32 v11, 0x1c00, v48
	s_and_b32 s0, s0, 0xffffff80
	ds_read2_b32 v[6:7], v6 offset0:8 offset1:137
	ds_read2_b32 v[38:39], v11 offset0:14 offset1:143
	s_waitcnt lgkmcnt(6)
	v_cvt_pk_bf16_f32 v2, v2, v3
	s_waitcnt lgkmcnt(5)
	v_cvt_pk_bf16_f32 v3, v4, v5
	s_waitcnt lgkmcnt(4)
	v_cvt_pk_bf16_f32 v5, v12, v13
	v_or_b32_e32 v12, s0, v42
	v_ashrrev_i32_e32 v13, 31, v12
	v_lshlrev_b64 v[12:13], 8, v[12:13]
	s_sub_i32 s4, s18, s0
	v_lshl_add_u64 v[12:13], s[14:15], 0, v[12:13]
	s_ashr_i32 s5, s4, 31
	v_lshl_add_u64 v[12:13], s[4:5], 1, v[12:13]
	v_mov_b32_e32 v11, v37
	s_waitcnt lgkmcnt(1)
	v_cvt_pk_bf16_f32 v6, v6, v7
	v_cvt_pk_bf16_f32 v7, v14, v15
	v_cvt_pk_bf16_f32 v4, v8, v9
	v_cvt_pk_bf16_f32 v8, v16, v17
	s_waitcnt lgkmcnt(0)
	v_cvt_pk_bf16_f32 v9, v38, v39
	v_lshl_add_u64 v[12:13], v[12:13], 0, v[10:11]
	global_store_dwordx4 v[12:13], v[2:5], off
	global_store_dwordx4 v[12:13], v[6:9], off offset:16
	s_add_i32 s18, s18, s19
	s_waitcnt vmcnt(2)
	v_mov_b64_e32 v[2:3], v[18:19]
	v_mov_b64_e32 v[6:7], v[22:23]
	s_andn2_b64 vcc, exec, s[16:17]
	v_mov_b64_e32 v[8:9], v[24:25]
	v_mov_b64_e32 v[4:5], v[20:21]
	s_mov_b32 s22, s29
	v_mov_b32_e32 v14, v30
	v_mov_b32_e32 v15, v31
	v_mov_b32_e32 v16, v32
	v_mov_b32_e32 v17, v33
	v_mov_b32_e32 v35, v26
	v_mov_b32_e32 v11, v27
	v_mov_b32_e32 v12, v28
	v_mov_b32_e32 v13, v29
	s_barrier
	s_cbranch_vccz .LBB0_196

.LBB0_201:
	s_or_b64 exec, exec, s[4:5]
	s_add_u32 s10, s54, 0x5380000
	s_addc_u32 s11, s55, 0
	v_lshl_add_u32 v10, v1, 2, 0
	v_lshl_add_u32 v18, v42, 2, 0
	s_lshl_b32 s20, s33, 6
	v_mov_b32_e32 v37, 0
	s_lshl_b32 s19, s18, 6
	v_or_b32_e32 v34, s20, v44
	s_movk_i32 s21, 0x5f
	s_movk_i32 s22, 0x60
	s_movk_i32 s23, 0x800
	s_movk_i32 s26, 0x7b9
	v_add_u32_e32 v47, v10, v43
	v_add_u32_e32 v48, v18, v46
	v_lshlrev_b32_e32 v10, 1, v45
	s_waitcnt vmcnt(0)
	s_branch .LBB0_204

.LBB0_203:
	ds_write2_b32 v47, v2, v3 offset1:1
	ds_write2_b32 v47, v4, v5 offset0:2 offset1:3
	ds_write2_b32 v47, v6, v7 offset0:4 offset1:5
	ds_write2_b32 v47, v8, v9 offset0:6 offset1:7
	ds_write2_b32 v47, v35, v11 offset0:64 offset1:65
	ds_write2_b32 v47, v12, v13 offset0:66 offset1:67
	ds_write2_b32 v47, v14, v15 offset0:68 offset1:69
	ds_write2_b32 v47, v16, v17 offset0:70 offset1:71
	v_add_u32_e32 v6, 0x800, v48
	s_waitcnt lgkmcnt(0)
	s_barrier
	v_add_u32_e32 v4, 0x400, v48
	ds_read2_b32 v[8:9], v6 offset0:4 offset1:133
	v_add_u32_e32 v6, 0xc00, v48
	ds_read2_b32 v[2:3], v48 offset1:129
	ds_read2_b32 v[4:5], v4 offset0:2 offset1:131
	ds_read2_b32 v[12:13], v6 offset0:6 offset1:135
	s_lshr_b32 s0, s18, 31
	s_add_i32 s0, s18, s0
	v_add_u32_e32 v11, 0x1400, v48
	ds_read2_b32 v[14:15], v11 offset0:10 offset1:139
	v_add_u32_e32 v11, 0x1800, v48
	s_lshl_b32 s0, s0, 6
	v_add_u32_e32 v6, 0x1000, v48
	ds_read2_b32 v[16:17], v11 offset0:12 offset1:141
	v_add_u32_e32 v11, 0x1c00, v48
	s_and_b32 s0, s0, 0xffffff80
	ds_read2_b32 v[6:7], v6 offset0:8 offset1:137
	ds_read2_b32 v[38:39], v11 offset0:14 offset1:143
	s_waitcnt lgkmcnt(6)
	v_cvt_pk_bf16_f32 v2, v2, v3
	s_waitcnt lgkmcnt(5)
	v_cvt_pk_bf16_f32 v3, v4, v5
	s_waitcnt lgkmcnt(4)
	v_cvt_pk_bf16_f32 v5, v12, v13
	v_or_b32_e32 v12, s0, v42
	v_ashrrev_i32_e32 v13, 31, v12
	v_lshlrev_b64 v[12:13], 8, v[12:13]
	s_sub_i32 s4, s19, s0
	v_lshl_add_u64 v[12:13], s[10:11], 0, v[12:13]
	s_ashr_i32 s5, s4, 31
	v_lshl_add_u64 v[12:13], s[4:5], 1, v[12:13]
	v_mov_b32_e32 v11, v37
	s_waitcnt lgkmcnt(1)
	v_cvt_pk_bf16_f32 v6, v6, v7
	v_cvt_pk_bf16_f32 v7, v14, v15
	v_cvt_pk_bf16_f32 v4, v8, v9
	v_cvt_pk_bf16_f32 v8, v16, v17
	s_waitcnt lgkmcnt(0)
	v_cvt_pk_bf16_f32 v9, v38, v39
	v_lshl_add_u64 v[12:13], v[12:13], 0, v[10:11]
	global_store_dwordx4 v[12:13], v[2:5], off
	global_store_dwordx4 v[12:13], v[6:9], off offset:16
	s_add_i32 s19, s19, s20
	s_waitcnt vmcnt(2)
	v_mov_b64_e32 v[2:3], v[18:19]
	v_mov_b64_e32 v[6:7], v[22:23]
	s_andn2_b64 vcc, exec, s[14:15]
	v_mov_b64_e32 v[8:9], v[24:25]
	v_mov_b64_e32 v[4:5], v[20:21]
	s_mov_b32 s18, s27
	v_mov_b32_e32 v14, v30
	v_mov_b32_e32 v15, v31
	v_mov_b32_e32 v16, v32
	v_mov_b32_e32 v17, v33
	v_mov_b32_e32 v35, v26
	v_mov_b32_e32 v11, v27
	v_mov_b32_e32 v12, v28
	v_mov_b32_e32 v13, v29
	s_barrier
	s_cbranch_vccz .LBB0_209

.LBB0_214:
	s_or_b64 exec, exec, s[4:5]
	s_add_u32 s10, s54, 0x5000000
	s_addc_u32 s11, s55, 0
	v_lshl_add_u32 v10, v1, 2, 0
	v_lshl_add_u32 v18, v42, 2, 0
	s_lshl_b32 s20, s33, 6
	v_mov_b32_e32 v37, 0
	s_lshl_b32 s19, s18, 6
	v_or_b32_e32 v34, s20, v44
	s_movk_i32 s21, 0x7ff
	s_movk_i32 s22, 0x800
	s_movk_i32 s23, 0xf9
	s_movk_i32 s26, 0xb9
	v_add_u32_e32 v47, v10, v43
	v_add_u32_e32 v48, v18, v46
	v_lshlrev_b32_e32 v10, 1, v45
	s_waitcnt vmcnt(0)
	s_branch .LBB0_217

.LBB0_216:
	ds_write2_b32 v47, v2, v3 offset1:1
	ds_write2_b32 v47, v4, v5 offset0:2 offset1:3
	ds_write2_b32 v47, v6, v7 offset0:4 offset1:5
	ds_write2_b32 v47, v8, v9 offset0:6 offset1:7
	ds_write2_b32 v47, v35, v11 offset0:64 offset1:65
	ds_write2_b32 v47, v12, v13 offset0:66 offset1:67
	ds_write2_b32 v47, v14, v15 offset0:68 offset1:69
	ds_write2_b32 v47, v16, v17 offset0:70 offset1:71
	v_add_u32_e32 v6, 0x800, v48
	s_waitcnt lgkmcnt(0)
	s_barrier
	v_add_u32_e32 v4, 0x400, v48
	ds_read2_b32 v[8:9], v6 offset0:4 offset1:133
	v_add_u32_e32 v6, 0xc00, v48
	ds_read2_b32 v[2:3], v48 offset1:129
	ds_read2_b32 v[4:5], v4 offset0:2 offset1:131
	ds_read2_b32 v[12:13], v6 offset0:6 offset1:135
	s_ashr_i32 s0, s18, 31
	s_lshr_b32 s0, s0, 27
	v_add_u32_e32 v11, 0x1400, v48
	s_add_i32 s0, s18, s0
	ds_read2_b32 v[14:15], v11 offset0:10 offset1:139
	v_add_u32_e32 v11, 0x1800, v48
	s_ashr_i32 s0, s0, 5
	v_add_u32_e32 v6, 0x1000, v48
	ds_read2_b32 v[16:17], v11 offset0:12 offset1:141
	v_add_u32_e32 v11, 0x1c00, v48
	ds_read2_b32 v[6:7], v6 offset0:8 offset1:137
	ds_read2_b32 v[38:39], v11 offset0:14 offset1:143
	s_waitcnt lgkmcnt(6)
	v_cvt_pk_bf16_f32 v2, v2, v3
	s_waitcnt lgkmcnt(5)
	v_cvt_pk_bf16_f32 v3, v4, v5
	s_waitcnt lgkmcnt(4)
	v_cvt_pk_bf16_f32 v5, v12, v13
	v_lshl_or_b32 v12, s0, 7, v42
	v_ashrrev_i32_e32 v13, 31, v12
	s_lshl_b32 s0, s0, 11
	v_lshlrev_b64 v[12:13], 12, v[12:13]
	s_sub_i32 s4, s19, s0
	v_lshl_add_u64 v[12:13], s[10:11], 0, v[12:13]
	s_ashr_i32 s5, s4, 31
	v_lshl_add_u64 v[12:13], s[4:5], 1, v[12:13]
	v_mov_b32_e32 v11, v37
	s_waitcnt lgkmcnt(1)
	v_cvt_pk_bf16_f32 v6, v6, v7
	v_cvt_pk_bf16_f32 v7, v14, v15
	v_cvt_pk_bf16_f32 v4, v8, v9
	v_cvt_pk_bf16_f32 v8, v16, v17
	s_waitcnt lgkmcnt(0)
	v_cvt_pk_bf16_f32 v9, v38, v39
	v_lshl_add_u64 v[12:13], v[12:13], 0, v[10:11]
	global_store_dwordx4 v[12:13], v[2:5], off
	global_store_dwordx4 v[12:13], v[6:9], off offset:16
	s_add_i32 s19, s19, s20
	s_waitcnt vmcnt(2)
	v_mov_b64_e32 v[2:3], v[18:19]
	v_mov_b64_e32 v[6:7], v[22:23]
	s_andn2_b64 vcc, exec, s[14:15]
	v_mov_b64_e32 v[8:9], v[24:25]
	v_mov_b64_e32 v[4:5], v[20:21]
	s_mov_b32 s18, s27
	v_mov_b32_e32 v14, v30
	v_mov_b32_e32 v15, v31
	v_mov_b32_e32 v16, v32
	v_mov_b32_e32 v17, v33
	v_mov_b32_e32 v35, v26
	v_mov_b32_e32 v11, v27
	v_mov_b32_e32 v12, v28
	v_mov_b32_e32 v13, v29
	s_barrier
	s_cbranch_vccz .LBB0_222

.LBB0_227:
	s_or_b64 exec, exec, s[4:5]
	s_add_u32 s10, s54, 0x5500000
	s_addc_u32 s11, s55, 0
	v_lshl_add_u32 v10, v1, 2, 0
	v_lshl_add_u32 v18, v42, 2, 0
	s_lshl_b32 s17, s33, 6
	v_mov_b32_e32 v37, 0
	s_lshl_b32 s16, s3, 6
	v_or_b32_e32 v34, s17, v44
	s_movk_i32 s18, 0xff
	s_movk_i32 s19, 0x100
	s_movk_i32 s20, 0x7f9
	s_movk_i32 s21, 0x7b9
	v_add_u32_e32 v43, v10, v43
	v_add_u32_e32 v44, v18, v46
	v_lshlrev_b32_e32 v10, 1, v45
	s_waitcnt vmcnt(0)
	s_branch .LBB0_230

.LBB0_229:
	ds_write2_b32 v43, v2, v3 offset1:1
	ds_write2_b32 v43, v4, v5 offset0:2 offset1:3
	ds_write2_b32 v43, v6, v7 offset0:4 offset1:5
	ds_write2_b32 v43, v8, v9 offset0:6 offset1:7
	ds_write2_b32 v43, v35, v11 offset0:64 offset1:65
	ds_write2_b32 v43, v12, v13 offset0:66 offset1:67
	ds_write2_b32 v43, v14, v15 offset0:68 offset1:69
	ds_write2_b32 v43, v16, v17 offset0:70 offset1:71
	v_add_u32_e32 v6, 0x800, v44
	s_waitcnt lgkmcnt(0)
	s_barrier
	v_add_u32_e32 v4, 0x400, v44
	ds_read2_b32 v[8:9], v6 offset0:4 offset1:133
	v_add_u32_e32 v6, 0xc00, v44
	ds_read2_b32 v[2:3], v44 offset1:129
	ds_read2_b32 v[4:5], v4 offset0:2 offset1:131
	ds_read2_b32 v[12:13], v6 offset0:6 offset1:135
	s_ashr_i32 s0, s3, 31
	s_lshr_b32 s0, s0, 30
	v_add_u32_e32 v11, 0x1400, v44
	s_add_i32 s0, s3, s0
	ds_read2_b32 v[14:15], v11 offset0:10 offset1:139
	v_add_u32_e32 v11, 0x1800, v44
	s_ashr_i32 s0, s0, 2
	v_add_u32_e32 v6, 0x1000, v44
	ds_read2_b32 v[16:17], v11 offset0:12 offset1:141
	v_add_u32_e32 v11, 0x1c00, v44
	ds_read2_b32 v[6:7], v6 offset0:8 offset1:137
	ds_read2_b32 v[38:39], v11 offset0:14 offset1:143
	s_waitcnt lgkmcnt(6)
	v_cvt_pk_bf16_f32 v2, v2, v3
	s_waitcnt lgkmcnt(5)
	v_cvt_pk_bf16_f32 v3, v4, v5
	s_waitcnt lgkmcnt(4)
	v_cvt_pk_bf16_f32 v5, v12, v13
	v_lshl_or_b32 v12, s0, 7, v42
	v_ashrrev_i32_e32 v13, 31, v12
	s_lshl_b32 s0, s0, 8
	v_lshlrev_b64 v[12:13], 9, v[12:13]
	s_sub_i32 s4, s16, s0
	v_lshl_add_u64 v[12:13], s[10:11], 0, v[12:13]
	s_ashr_i32 s5, s4, 31
	v_lshl_add_u64 v[12:13], s[4:5], 1, v[12:13]
	v_mov_b32_e32 v11, v37
	s_waitcnt lgkmcnt(1)
	v_cvt_pk_bf16_f32 v6, v6, v7
	v_cvt_pk_bf16_f32 v7, v14, v15
	v_cvt_pk_bf16_f32 v4, v8, v9
	v_cvt_pk_bf16_f32 v8, v16, v17
	s_waitcnt lgkmcnt(0)
	v_cvt_pk_bf16_f32 v9, v38, v39
	v_lshl_add_u64 v[12:13], v[12:13], 0, v[10:11]
	global_store_dwordx4 v[12:13], v[2:5], off
	global_store_dwordx4 v[12:13], v[6:9], off offset:16
	s_add_i32 s16, s16, s17
	s_waitcnt vmcnt(2)
	v_mov_b64_e32 v[2:3], v[18:19]
	v_mov_b64_e32 v[6:7], v[22:23]
	s_and_b64 vcc, exec, s[14:15]
	v_mov_b64_e32 v[8:9], v[24:25]
	v_mov_b64_e32 v[4:5], v[20:21]
	s_mov_b32 s3, s22
	v_mov_b32_e32 v14, v30
	v_mov_b32_e32 v15, v31
	v_mov_b32_e32 v16, v32
	v_mov_b32_e32 v17, v33
	v_mov_b32_e32 v35, v26
	v_mov_b32_e32 v11, v27
	v_mov_b32_e32 v12, v28
	v_mov_b32_e32 v13, v29
	s_barrier
	s_cbranch_vccnz .LBB0_235

.LBB0_433:
	s_or_b64 exec, exec, s[4:5]
	s_add_u32 s12, s54, 0x41800000
	s_addc_u32 s13, s55, 0
	v_lshl_add_u32 v10, v42, 2, 0
	v_mul_u32_u24_e32 v18, 0x204, v1
	v_lshl_add_u32 v19, v188, 2, 0
	v_mul_u32_u24_e32 v20, 0x204, v130
	s_lshl_b32 s19, s3, 6
	v_mov_b32_e32 v37, 0
	s_lshl_b32 s18, s16, 6
	v_or_b32_e32 v1, s19, v1
	s_movk_i32 s20, 0x1ff
	s_movk_i32 s21, 0x200
	s_movk_i32 s22, 0x800
	v_add_u32_e32 v34, v10, v18
	v_add_u32_e32 v43, v19, v20
	v_lshlrev_b32_e32 v10, 1, v130
	s_waitcnt vmcnt(0)
	s_branch .LBB0_436

.LBB0_435:
	ds_write2_b32 v34, v2, v3 offset1:1
	ds_write2_b32 v34, v4, v5 offset0:2 offset1:3
	ds_write2_b32 v34, v6, v7 offset0:4 offset1:5
	ds_write2_b32 v34, v8, v9 offset0:6 offset1:7
	ds_write2_b32 v34, v35, v11 offset0:64 offset1:65
	ds_write2_b32 v34, v12, v13 offset0:66 offset1:67
	ds_write2_b32 v34, v14, v15 offset0:68 offset1:69
	ds_write2_b32 v34, v16, v17 offset0:70 offset1:71
	v_add_u32_e32 v6, 0x800, v43
	s_waitcnt lgkmcnt(0)
	s_barrier
	v_add_u32_e32 v4, 0x400, v43
	ds_read2_b32 v[8:9], v6 offset0:4 offset1:133
	v_add_u32_e32 v6, 0xc00, v43
	ds_read2_b32 v[2:3], v43 offset1:129
	ds_read2_b32 v[4:5], v4 offset0:2 offset1:131
	ds_read2_b32 v[12:13], v6 offset0:6 offset1:135
	s_ashr_i32 s0, s16, 31
	s_lshr_b32 s0, s0, 29
	v_add_u32_e32 v11, 0x1400, v43
	s_add_i32 s0, s16, s0
	ds_read2_b32 v[14:15], v11 offset0:10 offset1:139
	v_add_u32_e32 v11, 0x1800, v43
	s_ashr_i32 s0, s0, 3
	v_add_u32_e32 v6, 0x1000, v43
	ds_read2_b32 v[16:17], v11 offset0:12 offset1:141
	v_add_u32_e32 v11, 0x1c00, v43
	ds_read2_b32 v[6:7], v6 offset0:8 offset1:137
	ds_read2_b32 v[38:39], v11 offset0:14 offset1:143
	s_waitcnt lgkmcnt(6)
	v_cvt_pk_bf16_f32 v2, v2, v3
	s_waitcnt lgkmcnt(5)
	v_cvt_pk_bf16_f32 v3, v4, v5
	s_waitcnt lgkmcnt(4)
	v_cvt_pk_bf16_f32 v5, v12, v13
	v_lshl_or_b32 v12, s0, 7, v188
	v_ashrrev_i32_e32 v13, 31, v12
	s_lshl_b32 s0, s0, 9
	v_lshlrev_b64 v[12:13], 10, v[12:13]
	s_sub_i32 s4, s18, s0
	v_lshl_add_u64 v[12:13], s[12:13], 0, v[12:13]
	s_ashr_i32 s5, s4, 31
	v_lshl_add_u64 v[12:13], s[4:5], 1, v[12:13]
	v_mov_b32_e32 v11, v37
	s_waitcnt lgkmcnt(1)
	v_cvt_pk_bf16_f32 v6, v6, v7
	v_cvt_pk_bf16_f32 v7, v14, v15
	v_cvt_pk_bf16_f32 v4, v8, v9
	v_cvt_pk_bf16_f32 v8, v16, v17
	s_waitcnt lgkmcnt(0)
	v_cvt_pk_bf16_f32 v9, v38, v39
	v_lshl_add_u64 v[12:13], v[12:13], 0, v[10:11]
	global_store_dwordx4 v[12:13], v[2:5], off
	global_store_dwordx4 v[12:13], v[6:9], off offset:16
	s_add_i32 s18, s18, s19
	s_waitcnt vmcnt(2)
	v_mov_b64_e32 v[2:3], v[18:19]
	v_mov_b64_e32 v[6:7], v[22:23]
	s_andn2_b64 vcc, exec, s[14:15]
	v_mov_b64_e32 v[8:9], v[24:25]
	v_mov_b64_e32 v[4:5], v[20:21]
	s_mov_b32 s16, s23
	v_mov_b32_e32 v14, v30
	v_mov_b32_e32 v15, v31
	v_mov_b32_e32 v16, v32
	v_mov_b32_e32 v17, v33
	v_mov_b32_e32 v35, v26
	v_mov_b32_e32 v11, v27
	v_mov_b32_e32 v12, v28
	v_mov_b32_e32 v13, v29
	s_barrier
	s_cbranch_vccz .LBB0_441

.LBB0_721:
	s_or_b64 exec, exec, s[4:5]
	s_add_u32 s10, s54, 0x39800000
	s_addc_u32 s11, s55, 0
	v_lshl_add_u32 v10, v44, 2, 0
	v_mul_u32_u24_e32 v18, 0x204, v1
	v_lshl_add_u32 v19, v188, 2, 0
	v_mul_u32_u24_e32 v20, 0x204, v146
	s_lshl_b32 s17, s3, 6
	v_mov_b32_e32 v39, 0
	s_lshl_b32 s16, s14, 6
	v_or_b32_e32 v1, s17, v1
	s_movk_i32 s18, 0x7ff
	s_movk_i32 s19, 0x800
	s_movk_i32 s20, 0xffd0
	s_movk_i32 s21, 0x200
	v_add_u32_e32 v36, v10, v18
	v_add_u32_e32 v46, v19, v20
	v_lshlrev_b32_e32 v10, 1, v146
	s_waitcnt vmcnt(0)
	s_branch .LBB0_724

.LBB0_723:
	ds_write2_b32 v36, v2, v3 offset1:1
	ds_write2_b32 v36, v4, v5 offset0:2 offset1:3
	ds_write2_b32 v36, v6, v7 offset0:4 offset1:5
	ds_write2_b32 v36, v8, v9 offset0:6 offset1:7
	ds_write2_b32 v36, v37, v11 offset0:64 offset1:65
	ds_write2_b32 v36, v12, v13 offset0:66 offset1:67
	ds_write2_b32 v36, v14, v15 offset0:68 offset1:69
	ds_write2_b32 v36, v16, v17 offset0:70 offset1:71
	v_add_u32_e32 v6, 0x800, v46
	s_waitcnt lgkmcnt(0)
	s_barrier
	v_add_u32_e32 v4, 0x400, v46
	ds_read2_b32 v[8:9], v6 offset0:4 offset1:133
	v_add_u32_e32 v6, 0xc00, v46
	ds_read2_b32 v[2:3], v46 offset1:129
	ds_read2_b32 v[4:5], v4 offset0:2 offset1:131
	ds_read2_b32 v[12:13], v6 offset0:6 offset1:135
	s_ashr_i32 s0, s14, 31
	s_lshr_b32 s0, s0, 27
	v_add_u32_e32 v11, 0x1400, v46
	s_add_i32 s0, s14, s0
	ds_read2_b32 v[14:15], v11 offset0:10 offset1:139
	v_add_u32_e32 v11, 0x1800, v46
	s_ashr_i32 s0, s0, 5
	v_add_u32_e32 v6, 0x1000, v46
	ds_read2_b32 v[16:17], v11 offset0:12 offset1:141
	v_add_u32_e32 v11, 0x1c00, v46
	ds_read2_b32 v[6:7], v6 offset0:8 offset1:137
	ds_read2_b32 v[40:41], v11 offset0:14 offset1:143
	s_waitcnt lgkmcnt(6)
	v_cvt_pk_bf16_f32 v2, v2, v3
	s_waitcnt lgkmcnt(5)
	v_cvt_pk_bf16_f32 v3, v4, v5
	s_waitcnt lgkmcnt(4)
	v_cvt_pk_bf16_f32 v5, v12, v13
	v_lshl_or_b32 v12, s0, 7, v188
	v_ashrrev_i32_e32 v13, 31, v12
	s_lshl_b32 s0, s0, 11
	v_lshlrev_b64 v[12:13], 12, v[12:13]
	s_sub_i32 s4, s16, s0
	v_lshl_add_u64 v[12:13], s[10:11], 0, v[12:13]
	s_ashr_i32 s5, s4, 31
	v_lshl_add_u64 v[12:13], s[4:5], 1, v[12:13]
	v_mov_b32_e32 v11, v39
	s_waitcnt lgkmcnt(1)
	v_cvt_pk_bf16_f32 v6, v6, v7
	v_cvt_pk_bf16_f32 v7, v14, v15
	v_cvt_pk_bf16_f32 v4, v8, v9
	v_cvt_pk_bf16_f32 v8, v16, v17
	s_waitcnt lgkmcnt(0)
	v_cvt_pk_bf16_f32 v9, v40, v41
	v_lshl_add_u64 v[12:13], v[12:13], 0, v[10:11]
	global_store_dwordx4 v[12:13], v[2:5], off
	global_store_dwordx4 v[12:13], v[6:9], off offset:16
	s_add_i32 s16, s16, s17
	s_waitcnt vmcnt(2)
	v_mov_b64_e32 v[2:3], v[18:19]
	v_mov_b64_e32 v[6:7], v[22:23]
	s_andn2_b64 vcc, exec, s[12:13]
	v_mov_b64_e32 v[8:9], v[24:25]
	v_mov_b64_e32 v[4:5], v[20:21]
	s_mov_b32 s14, s22
	v_mov_b32_e32 v14, v30
	v_mov_b32_e32 v15, v31
	v_mov_b32_e32 v16, v32
	v_mov_b32_e32 v17, v33
	v_mov_b32_e32 v37, v26
	v_mov_b32_e32 v11, v27
	v_mov_b32_e32 v12, v28
	v_mov_b32_e32 v13, v29
	s_barrier
	s_cbranch_vccz .LBB0_729

.LBB0_1808:
	s_or_b64 exec, exec, s[4:5]
	s_add_u32 s8, s54, 0x41a00000
	s_addc_u32 s9, s55, 0
	v_lshl_add_u32 v10, v1, 2, 0
	v_mul_u32_u24_e32 v18, 0x204, v131
	v_lshl_add_u32 v19, v188, 2, 0
	v_mul_u32_u24_e32 v20, 0x204, v130
	s_lshl_b32 s15, s3, 6
	v_mov_b32_e32 v39, 0
	s_lshl_b32 s14, s12, 6
	v_or_b32_e32 v36, s15, v131
	s_movk_i32 s16, 0x7ff
	s_movk_i32 s17, 0x800
	s_movk_i32 s18, 0xffd0
	s_movk_i32 s19, 0x200
	v_add_u32_e32 v45, v10, v18
	v_add_u32_e32 v46, v19, v20
	v_lshlrev_b32_e32 v10, 1, v130
	s_waitcnt vmcnt(0)
	s_branch .LBB0_1811

.LBB0_1810:
	ds_write2_b32 v45, v2, v3 offset1:1
	ds_write2_b32 v45, v4, v5 offset0:2 offset1:3
	ds_write2_b32 v45, v6, v7 offset0:4 offset1:5
	ds_write2_b32 v45, v8, v9 offset0:6 offset1:7
	ds_write2_b32 v45, v37, v11 offset0:64 offset1:65
	ds_write2_b32 v45, v12, v13 offset0:66 offset1:67
	ds_write2_b32 v45, v14, v15 offset0:68 offset1:69
	ds_write2_b32 v45, v16, v17 offset0:70 offset1:71
	v_add_u32_e32 v6, 0x800, v46
	s_waitcnt lgkmcnt(0)
	s_barrier
	v_add_u32_e32 v4, 0x400, v46
	ds_read2_b32 v[8:9], v6 offset0:4 offset1:133
	v_add_u32_e32 v6, 0xc00, v46
	ds_read2_b32 v[2:3], v46 offset1:129
	ds_read2_b32 v[4:5], v4 offset0:2 offset1:131
	ds_read2_b32 v[12:13], v6 offset0:6 offset1:135
	s_ashr_i32 s0, s12, 31
	s_lshr_b32 s0, s0, 27
	v_add_u32_e32 v11, 0x1400, v46
	s_add_i32 s0, s12, s0
	ds_read2_b32 v[14:15], v11 offset0:10 offset1:139
	v_add_u32_e32 v11, 0x1800, v46
	s_ashr_i32 s0, s0, 5
	v_add_u32_e32 v6, 0x1000, v46
	ds_read2_b32 v[16:17], v11 offset0:12 offset1:141
	v_add_u32_e32 v11, 0x1c00, v46
	ds_read2_b32 v[6:7], v6 offset0:8 offset1:137
	ds_read2_b32 v[40:41], v11 offset0:14 offset1:143
	s_waitcnt lgkmcnt(6)
	v_cvt_pk_bf16_f32 v2, v2, v3
	s_waitcnt lgkmcnt(5)
	v_cvt_pk_bf16_f32 v3, v4, v5
	s_waitcnt lgkmcnt(4)
	v_cvt_pk_bf16_f32 v5, v12, v13
	v_lshl_or_b32 v12, s0, 7, v188
	v_ashrrev_i32_e32 v13, 31, v12
	s_lshl_b32 s0, s0, 11
	v_lshlrev_b64 v[12:13], 12, v[12:13]
	s_sub_i32 s0, s14, s0
	v_lshl_add_u64 v[12:13], s[8:9], 0, v[12:13]
	s_ashr_i32 s1, s0, 31
	v_lshl_add_u64 v[12:13], s[0:1], 1, v[12:13]
	v_mov_b32_e32 v11, v39
	s_waitcnt lgkmcnt(1)
	v_cvt_pk_bf16_f32 v6, v6, v7
	v_cvt_pk_bf16_f32 v7, v14, v15
	v_cvt_pk_bf16_f32 v4, v8, v9
	v_cvt_pk_bf16_f32 v8, v16, v17
	s_waitcnt lgkmcnt(0)
	v_cvt_pk_bf16_f32 v9, v40, v41
	v_lshl_add_u64 v[12:13], v[12:13], 0, v[10:11]
	global_store_dwordx4 v[12:13], v[2:5], off
	global_store_dwordx4 v[12:13], v[6:9], off offset:16
	s_add_i32 s14, s14, s15
	s_waitcnt vmcnt(2)
	v_mov_b64_e32 v[2:3], v[18:19]
	v_mov_b64_e32 v[6:7], v[22:23]
	s_andn2_b64 vcc, exec, s[10:11]
	v_mov_b64_e32 v[8:9], v[24:25]
	v_mov_b64_e32 v[4:5], v[20:21]
	s_mov_b32 s12, s20
	v_mov_b32_e32 v14, v30
	v_mov_b32_e32 v15, v31
	v_mov_b32_e32 v16, v32
	v_mov_b32_e32 v17, v33
	v_mov_b32_e32 v37, v26
	v_mov_b32_e32 v11, v27
	v_mov_b32_e32 v12, v28
	v_mov_b32_e32 v13, v29
	s_barrier
	s_cbranch_vccz .Lx14_begin

.LBB0_2008:
	s_or_b64 exec, exec, s[38:39]
	s_lshl_b32 s45, s33, 6
	s_lshl_b32 s44, s3, 6
	v_add_u32_e32 v40, s45, v1
	s_mov_b32 s46, s3
	s_waitcnt vmcnt(0)
	s_branch .LBB0_2011

.LBB0_2010:
	v_add_u32_e32 v2, 0x400, v196
	ds_write2_b32 v195, v8, v9 offset1:1
	ds_write2_b32 v195, v10, v11 offset0:2 offset1:3
	ds_write2_b32 v195, v4, v5 offset0:4 offset1:5
	ds_write2_b32 v195, v6, v7 offset0:6 offset1:7
	ds_write2_b32 v195, v16, v17 offset0:64 offset1:65
	ds_write2_b32 v195, v18, v19 offset0:66 offset1:67
	ds_write2_b32 v195, v12, v13 offset0:68 offset1:69
	ds_write2_b32 v195, v14, v15 offset0:70 offset1:71
	s_waitcnt lgkmcnt(0)
	s_barrier
	ds_read2_b32 v[6:7], v2 offset0:2 offset1:131
	v_add_u32_e32 v2, 0x800, v196
	ds_read2_b32 v[10:11], v2 offset0:4 offset1:133
	v_add_u32_e32 v2, 0xc00, v196
	ds_read2_b32 v[4:5], v196 offset1:129
	ds_read2_b32 v[12:13], v2 offset0:6 offset1:135
	s_ashr_i32 s38, s46, 31
	v_add_u32_e32 v2, 0x1000, v196
	s_lshr_b32 s38, s38, 29
	ds_read2_b32 v[8:9], v2 offset0:8 offset1:137
	v_add_u32_e32 v2, 0x1400, v196
	s_add_i32 s38, s46, s38
	ds_read2_b32 v[14:15], v2 offset0:10 offset1:139
	v_add_u32_e32 v2, 0x1800, v196
	s_ashr_i32 s38, s38, 3
	ds_read2_b32 v[16:17], v2 offset0:12 offset1:141
	v_add_u32_e32 v2, 0x1c00, v196
	ds_read2_b32 v[18:19], v2 offset0:14 offset1:143
	s_waitcnt lgkmcnt(5)
	v_cvt_pk_bf16_f32 v4, v4, v5
	v_cvt_pk_bf16_f32 v5, v6, v7
	s_waitcnt lgkmcnt(4)
	v_cvt_pk_bf16_f32 v7, v12, v13
	v_lshl_add_u32 v12, s38, 7, v188
	v_ashrrev_i32_e32 v13, 31, v12
	s_lshl_b32 s38, s38, 9
	v_lshlrev_b64 v[12:13], 10, v[12:13]
	s_sub_i32 s38, s44, s38
	v_lshl_add_u64 v[12:13], s[58:59], 0, v[12:13]
	s_ashr_i32 s39, s38, 31
	v_lshl_add_u64 v[12:13], s[38:39], 1, v[12:13]
	v_mov_b32_e32 v163, v3
	s_waitcnt lgkmcnt(3)
	v_cvt_pk_bf16_f32 v8, v8, v9
	s_waitcnt lgkmcnt(2)
	v_cvt_pk_bf16_f32 v9, v14, v15
	v_cvt_pk_bf16_f32 v6, v10, v11
	s_waitcnt lgkmcnt(1)
	v_cvt_pk_bf16_f32 v10, v16, v17
	s_waitcnt lgkmcnt(0)
	v_cvt_pk_bf16_f32 v11, v18, v19
	v_lshl_add_u64 v[12:13], v[12:13], 0, v[162:163]
	global_store_dwordx4 v[12:13], v[4:7], off
	global_store_dwordx4 v[12:13], v[8:11], off offset:16
	s_add_i32 s44, s44, s45
	s_waitcnt vmcnt(2)
	v_mov_b64_e32 v[4:5], v[24:25]
	v_mov_b64_e32 v[8:9], v[20:21]
	s_andn2_b64 vcc, exec, s[42:43]
	v_mov_b64_e32 v[6:7], v[26:27]
	v_mov_b64_e32 v[10:11], v[22:23]
	s_mov_b32 s46, s47
	v_mov_b32_e32 v12, v32
	v_mov_b32_e32 v13, v33
	v_mov_b32_e32 v14, v34
	v_mov_b32_e32 v15, v35
	v_mov_b32_e32 v16, v28
	v_mov_b32_e32 v17, v29
	v_mov_b32_e32 v18, v30
	v_mov_b32_e32 v19, v31
	s_barrier
	s_cbranch_vccz .LBB0_2016
